# att10: per-tile bookkeeping (next-half load and K-read addresses, row-sum update, pointer advance) moved from behind the last PV MFMA into the MFMA gaps of PV blocks 1-3
# baseline (speedup 1.0000x reference)
; __device__ __forceinline__ void qkt64c(f32x16& p0, f32x16& p1, const char* Ks, const bf16x8* qr, const f32x16& cinit, int r32, int hi) {
; #pragma unroll
;     for (int d0 = 0; d0 < 4; ++d0) { const int cb = (d0 * 16 + hi * 8) * 2;
;         const bf16x8 b0 = *reinterpret_cast<const bf16x8*>(Ks + kswz<64>(r32, cb));
;         const bf16x8 b1 = *reinterpret_cast<const bf16x8*>(Ks + kswz<64>(32 + r32, cb));
;         if (d0 == 0) { p0 = __builtin_amdgcn_mfma_f32_32x32x16_bf16(b0, qr[0], cinit, 0, 0, 0); p1 = __builtin_amdgcn_mfma_f32_32x32x16_bf16(b1, qr[0], cinit, 0, 0, 0); }
;         else { p0 = __builtin_amdgcn_mfma_f32_32x32x16_bf16(b0, qr[d0], p0, 0, 0, 0); p1 = __builtin_amdgcn_mfma_f32_32x32x16_bf16(b1, qr[d0], p1, 0, 0, 0); } }
; }
.LBB0_823:
	s_lshl_b32 s2, s42, 13
	s_add_i32 s2, s2, 0
	v_add_u32_e32 v72, s2, v223
	v_add_u32_e32 v73, s2, v226
	v_add_u32_e32 v74, s2, v228
	v_add_u32_e32 v75, s2, v229
.Latt9_p1_top:
	ds_read_b128 v[144:147], v72 offset:49152
	ds_read_b128 v[148:151], v73 offset:49152
	ds_read_b128 v[152:155], v74 offset:49152
	ds_read_b128 v[156:159], v75 offset:49152
	ds_read_b128 v[232:235], v72 offset:53248
	ds_read_b128 v[236:239], v73 offset:53248
	ds_read_b128 v[240:243], v74 offset:53248
	ds_read_b128 v[244:247], v75 offset:53248
	v_lshl_add_u64 v[202:203], v[200:201], 0, s[64:65]
	s_mov_b32 s2, 0x8a40000
	v_add_co_u32_e32 v64, vcc, s2, v202
	s_mov_b32 s2, 0x8a50000
	s_nop 0
	v_addc_co_u32_e32 v65, vcc, 0, v203, vcc
	v_add_co_u32_e32 v66, vcc, s2, v202
	v_lshl_add_u64 v[204:205], v[198:199], 0, s[64:65]
	s_nop 0
	v_addc_co_u32_e32 v67, vcc, 0, v203, vcc
	s_mov_b32 s2, 0x6a40000
	global_load_dwordx4 v[178:181], v[64:65], off
	global_load_dwordx4 v[182:185], v[66:67], off
	v_add_co_u32_e32 v64, vcc, s2, v204
	s_nop 1
	v_addc_co_u32_e32 v65, vcc, 0, v205, vcc
	global_load_dwordx4 v[186:189], v[64:65], off
	v_exp_f32_e32 v190, v120
	v_exp_f32_e32 v191, v121
	v_add_f32_e32 v120, v96, v97
	v_add_f32_e32 v121, v98, v99
	s_waitcnt lgkmcnt(7)
	v_mfma_f32_32x32x16_bf16 v[128:143], v[144:147], v[162:165], v[80:95]
	v_exp_f32_e32 v192, v122
	v_add_f32_e32 v120, v120, v121
	v_add_f32_e32 v121, v100, v101
	v_add_f32_e32 v122, v102, v103
	v_exp_f32_e32 v193, v123
	s_waitcnt lgkmcnt(6)
	v_mfma_f32_32x32x16_bf16 v[128:143], v[148:151], v[166:169], v[128:143]
	v_add_f32_e32 v121, v121, v122
	v_add_f32_e32 v122, v104, v105
	v_add_f32_e32 v123, v106, v107
	v_add_f32_e32 v122, v122, v123
	v_add_f32_e32 v123, v108, v109
	s_waitcnt lgkmcnt(5)
	v_mfma_f32_32x32x16_bf16 v[128:143], v[152:155], v[170:173], v[128:143]
	v_add_f32_e32 v208, v110, v111
	v_add_f32_e32 v123, v123, v208
	v_add_f32_e32 v208, v112, v113
	v_add_f32_e32 v209, v114, v115
	v_add_f32_e32 v208, v208, v209
	s_waitcnt lgkmcnt(4)
	v_mfma_f32_32x32x16_bf16 v[128:143], v[156:159], v[174:177], v[128:143]
	v_exp_f32_e32 v124, v124
	v_exp_f32_e32 v125, v125
	s_waitcnt lgkmcnt(3)
	v_mfma_f32_32x32x16_bf16 v[144:159], v[232:235], v[162:165], v[80:95]
	v_lshl_add_u32 v234, s12, 14, v217
	ds_read_b64_tr_b16 v[64:65], v234 offset:0
	ds_read_b64_tr_b16 v[66:67], v234 offset:0x800
	ds_read_b64_tr_b16 v[68:69], v234 offset:0x1000
	ds_read_b64_tr_b16 v[70:71], v234 offset:0x1800
	ds_read_b64_tr_b16 v[72:73], v234 offset:0x2000
	ds_read_b64_tr_b16 v[74:75], v234 offset:0x2800
	ds_read_b64_tr_b16 v[76:77], v234 offset:0x3000
	ds_read_b64_tr_b16 v[78:79], v234 offset:0x3800
	v_exp_f32_e32 v126, v126
	v_exp_f32_e32 v127, v127
	v_add_f32_e32 v120, v208, v120
	v_add_f32_e32 v208, v116, v117
	v_add_f32_e32 v209, v118, v119
	v_add_f32_e32 v208, v208, v209
	v_add_f32_e32 v121, v208, v121
	s_waitcnt lgkmcnt(10)
	v_mfma_f32_32x32x16_bf16 v[144:159], v[236:239], v[166:169], v[144:159]
	v_add_f32_e32 v208, v190, v191
	v_add_f32_e32 v209, v192, v193
	v_add_f32_e32 v208, v208, v209
	v_add_f32_e32 v122, v122, v208
	v_add_f32_e32 v208, v124, v125
	v_add_f32_e32 v209, v126, v127
	v_add_f32_e32 v208, v208, v209
	s_waitcnt lgkmcnt(9)
	v_mfma_f32_32x32x16_bf16 v[144:159], v[240:243], v[170:173], v[144:159]
	v_add_f32_e32 v123, v123, v208
	v_add_f32_e32 v120, v120, v121
	v_add_f32_e32 v121, v122, v123
	v_add_f32_e32 v231, v120, v121
	v_mov_b32_e32 v232, v231
	v_cvt_pk_bf16_f32 v96, v96, v97
	v_cvt_pk_bf16_f32 v97, v98, v99
	s_waitcnt lgkmcnt(8)
	v_mfma_f32_32x32x16_bf16 v[144:159], v[244:247], v[174:177], v[144:159]
	v_cvt_pk_bf16_f32 v98, v100, v101
	v_cvt_pk_bf16_f32 v99, v102, v103
	v_cvt_pk_bf16_f32 v120, v104, v105
	v_cvt_pk_bf16_f32 v121, v106, v107
	v_cvt_pk_bf16_f32 v122, v108, v109
	v_cvt_pk_bf16_f32 v123, v110, v111
	v_permlane32_swap_b32_e32 v96, v98
	v_permlane32_swap_b32_e32 v97, v99
	v_cvt_pk_bf16_f32 v104, v112, v113
	v_cvt_pk_bf16_f32 v105, v114, v115
	v_cvt_pk_bf16_f32 v106, v116, v117
	v_cvt_pk_bf16_f32 v107, v118, v119
	s_waitcnt lgkmcnt(0)
	v_mfma_f32_32x32x16_bf16 v[0:15], v[96:99], v[64:67], v[0:15]
	v_permlane32_swap_b32_e32 v120, v122
	v_permlane32_swap_b32_e32 v121, v123
	v_cvt_pk_bf16_f32 v100, v190, v191
	v_cvt_pk_bf16_f32 v101, v192, v193
	v_cvt_pk_bf16_f32 v102, v124, v125
	v_cvt_pk_bf16_f32 v103, v126, v127
	v_mfma_f32_32x32x16_bf16 v[0:15], v[120:123], v[68:71], v[0:15]
	v_permlane32_swap_b32_e32 v104, v106
	v_permlane32_swap_b32_e32 v105, v107
	ds_read_b64_tr_b16 v[236:237], v234 offset:0x200
	ds_read_b64_tr_b16 v[238:239], v234 offset:0xa00
	ds_read_b64_tr_b16 v[240:241], v234 offset:0x1200
	ds_read_b64_tr_b16 v[242:243], v234 offset:0x1a00
	ds_read_b64_tr_b16 v[244:245], v234 offset:0x2200
	ds_read_b64_tr_b16 v[246:247], v234 offset:0x2a00
	ds_read_b64_tr_b16 v[190:191], v234 offset:0x3200
	ds_read_b64_tr_b16 v[192:193], v234 offset:0x3a00
	v_mfma_f32_32x32x16_bf16 v[0:15], v[104:107], v[72:75], v[0:15]
	v_permlane32_swap_b32_e32 v100, v102
	v_permlane32_swap_b32_e32 v101, v103
	v_permlane32_swap_b32_e32 v231, v232
	v_max_f32_e32 v108, v128, v129
	v_max3_f32 v109, v130, v131, v145
	v_max3_f32 v108, v108, v144, v146
	v_max3_f32 v108, v108, v147, v132
	v_max3_f32 v109, v109, v134, v135
	v_mfma_f32_32x32x16_bf16 v[0:15], v[100:103], v[76:79], v[0:15]
	v_max3_f32 v208, v108, v133, v148
	v_max3_f32 v209, v109, v150, v151
	ds_read_b64_tr_b16 v[124:125], v234 offset:0x400
	ds_read_b64_tr_b16 v[126:127], v234 offset:0xc00
	ds_read_b64_tr_b16 v[116:117], v234 offset:0x1400
	ds_read_b64_tr_b16 v[118:119], v234 offset:0x1c00
	ds_read_b64_tr_b16 v[112:113], v234 offset:0x2400
	ds_read_b64_tr_b16 v[114:115], v234 offset:0x2c00
	ds_read_b64_tr_b16 v[108:109], v234 offset:0x3400
	ds_read_b64_tr_b16 v[110:111], v234 offset:0x3c00
	s_waitcnt lgkmcnt(8)
	v_mfma_f32_32x32x16_bf16 v[48:63], v[96:99], v[236:239], v[48:63]
	v_max3_f32 v208, v208, v149, v136
	v_max3_f32 v209, v209, v138, v139
	v_max3_f32 v208, v208, v137, v152
	v_max3_f32 v209, v209, v154, v155
	v_max3_f32 v208, v208, v153, v140
	v_max3_f32 v209, v209, v142, v143
	v_max3_f32 v208, v208, v141, v156
	v_mfma_f32_32x32x16_bf16 v[48:63], v[120:123], v[240:243], v[48:63]
	v_max3_f32 v209, v209, v158, v159
	v_max3_f32 v208, v208, v157, v209
	v_mov_b32_e32 v209, v208
	s_nop 1
	v_permlane32_swap_b32_e32 v208, v209
	v_mfma_f32_32x32x16_bf16 v[48:63], v[104:107], v[244:247], v[48:63]
	v_max_f32_e32 v233, v208, v209
	s_mov_b32 s2, 0x4138aa3b
	v_cmp_ge_f32_e32 vcc, s2, v233
	v_mfma_f32_32x32x16_bf16 v[48:63], v[100:103], v[190:193], v[48:63]
	s_cmp_eq_u64 vcc, exec
	s_cbranch_scc0 .LBB0_836
	v_mov_b32_e32 v233, 1.0
.LBB0_825:
	ds_read_b64_tr_b16 v[190:191], v234 offset:0x600
	ds_read_b64_tr_b16 v[192:193], v234 offset:0xe00
	ds_read_b64_tr_b16 v[236:237], v234 offset:0x1600
	ds_read_b64_tr_b16 v[238:239], v234 offset:0x1e00
	ds_read_b64_tr_b16 v[240:241], v234 offset:0x2600
	ds_read_b64_tr_b16 v[242:243], v234 offset:0x2e00
	ds_read_b64_tr_b16 v[244:245], v234 offset:0x3600
	ds_read_b64_tr_b16 v[246:247], v234 offset:0x3e00
	s_waitcnt lgkmcnt(8)
	v_mfma_f32_32x32x16_bf16 v[32:47], v[96:99], v[124:127], v[32:47]
	v_exp_f32_e32 v128, v128
	v_exp_f32_e32 v129, v129
	v_exp_f32_e32 v130, v130
	v_add_co_u32_e32 v66, vcc, 0x8a60000, v202
	s_nop 1
	v_addc_co_u32_e32 v67, vcc, 0, v203, vcc
	v_mfma_f32_32x32x16_bf16 v[32:47], v[120:123], v[116:119], v[32:47]
	v_exp_f32_e32 v131, v131
	v_exp_f32_e32 v132, v132
	v_exp_f32_e32 v133, v133
	v_add_co_u32_e32 v68, vcc, 0x8a70000, v202
	s_nop 1
	v_addc_co_u32_e32 v69, vcc, 0, v203, vcc
	v_mfma_f32_32x32x16_bf16 v[32:47], v[104:107], v[112:115], v[32:47]
	v_exp_f32_e32 v134, v134
	v_exp_f32_e32 v135, v135
	v_exp_f32_e32 v136, v136
	v_add_co_u32_e32 v70, vcc, 0x6a60000, v204
	s_nop 1
	v_addc_co_u32_e32 v71, vcc, 0, v205, vcc
	v_mfma_f32_32x32x16_bf16 v[32:47], v[100:103], v[108:111], v[32:47]
	v_exp_f32_e32 v137, v137
	v_exp_f32_e32 v138, v138
	v_exp_f32_e32 v139, v139
	s_waitcnt lgkmcnt(0)
	s_lshl_b32 s2, s41, 14
	s_add_i32 s2, s2, 0
	v_add_u32_e32 v64, s2, v218
	s_lshl_b32 s3, s41, 13
	s_waitcnt vmcnt(2)
	ds_write_b128 v64, v[178:181]
	v_add_u32_e32 v64, s2, v219
	s_sub_i32 s2, s2, s3
	s_waitcnt vmcnt(1)
	ds_write_b128 v64, v[182:185]
	v_add_u32_e32 v64, s2, v220
	s_waitcnt vmcnt(0)
	ds_write_b128 v64, v[186:189] offset:49152
	v_mfma_f32_32x32x16_bf16 v[16:31], v[96:99], v[190:193], v[16:31]
	v_exp_f32_e32 v140, v140
	v_exp_f32_e32 v141, v141
	v_exp_f32_e32 v142, v142
	v_add_u32_e32 v72, s2, v223
	v_add_u32_e32 v73, s2, v226
	v_mfma_f32_32x32x16_bf16 v[16:31], v[120:123], v[236:239], v[16:31]
	v_exp_f32_e32 v143, v143
	v_exp_f32_e32 v144, v144
	v_exp_f32_e32 v145, v145
	v_cmp_gt_f32_e32 vcc, 1.0, v233
	v_add_u32_e32 v74, s2, v228
	v_add_u32_e32 v75, s2, v229
	v_mfma_f32_32x32x16_bf16 v[16:31], v[104:107], v[240:243], v[16:31]
	v_exp_f32_e32 v146, v146
	v_exp_f32_e32 v147, v147
	v_exp_f32_e32 v148, v148
	v_mfma_f32_32x32x16_bf16 v[16:31], v[100:103], v[244:247], v[16:31]
	v_exp_f32_e32 v149, v149
	v_exp_f32_e32 v150, v150
	v_exp_f32_e32 v151, v151
	s_cbranch_vccz .LBB0_829
	s_and_saveexec_b64 s[12:13], s[0:1]
	ds_write_b32 v214, v233 offset:128
	s_or_b64 exec, exec, s[12:13]
	s_waitcnt lgkmcnt(0)
	v_add_u32_e32 v108, v213, v160
	ds_read_b128 v[96:99], v108 offset:224
	ds_read_b128 v[100:103], v108 offset:192
	ds_read_b128 v[104:107], v108 offset:160
	ds_read_b128 v[108:111], v108 offset:128
	s_waitcnt lgkmcnt(3)
	v_pk_mul_f32 v[12:13], v[12:13], v[96:97]
	s_waitcnt lgkmcnt(2)
	v_pk_mul_f32 v[8:9], v[8:9], v[100:101]
	s_waitcnt lgkmcnt(1)
	v_pk_mul_f32 v[4:5], v[4:5], v[104:105]
	v_pk_mul_f32 v[14:15], v[14:15], v[98:99]
	v_pk_mul_f32 v[10:11], v[10:11], v[102:103]
	v_pk_mul_f32 v[6:7], v[6:7], v[106:107]
	s_waitcnt lgkmcnt(0)
	v_pk_mul_f32 v[2:3], v[2:3], v[110:111]
	v_pk_mul_f32 v[0:1], v[0:1], v[108:109]
	v_pk_mul_f32 v[60:61], v[60:61], v[96:97]
	v_pk_mul_f32 v[56:57], v[56:57], v[100:101]
	v_pk_mul_f32 v[52:53], v[52:53], v[104:105]
	v_pk_mul_f32 v[62:63], v[62:63], v[98:99]
	v_pk_mul_f32 v[58:59], v[58:59], v[102:103]
	v_pk_mul_f32 v[54:55], v[54:55], v[106:107]
	v_pk_mul_f32 v[50:51], v[50:51], v[110:111]
	v_pk_mul_f32 v[48:49], v[48:49], v[108:109]
	v_pk_mul_f32 v[44:45], v[44:45], v[96:97]
	v_pk_mul_f32 v[40:41], v[40:41], v[100:101]
	v_pk_mul_f32 v[36:37], v[36:37], v[104:105]
	v_pk_mul_f32 v[46:47], v[46:47], v[98:99]
	v_pk_mul_f32 v[42:43], v[42:43], v[102:103]
	v_pk_mul_f32 v[38:39], v[38:39], v[106:107]
	v_pk_mul_f32 v[34:35], v[34:35], v[110:111]
	v_pk_mul_f32 v[32:33], v[32:33], v[108:109]
	v_pk_mul_f32 v[28:29], v[28:29], v[96:97]
	v_pk_mul_f32 v[24:25], v[24:25], v[100:101]
	v_pk_mul_f32 v[20:21], v[20:21], v[104:105]
	v_pk_mul_f32 v[30:31], v[30:31], v[98:99]
	v_pk_mul_f32 v[26:27], v[26:27], v[102:103]
	v_pk_mul_f32 v[22:23], v[22:23], v[106:107]
	v_pk_mul_f32 v[18:19], v[18:19], v[110:111]
	v_pk_mul_f32 v[16:17], v[16:17], v[108:109]
; __device__ __forceinline__ void qkt64c(f32x16& p0, f32x16& p1, const char* Ks, const bf16x8* qr, const f32x16& cinit, int r32, int hi) {
; #pragma unroll
;     for (int d0 = 0; d0 < 4; ++d0) { const int cb = (d0 * 16 + hi * 8) * 2;
;         const bf16x8 b0 = *reinterpret_cast<const bf16x8*>(Ks + kswz<64>(r32, cb));
;         const bf16x8 b1 = *reinterpret_cast<const bf16x8*>(Ks + kswz<64>(32 + r32, cb));
;         if (d0 == 0) { p0 = __builtin_amdgcn_mfma_f32_32x32x16_bf16(b0, qr[0], cinit, 0, 0, 0); p1 = __builtin_amdgcn_mfma_f32_32x32x16_bf16(b1, qr[0], cinit, 0, 0, 0); }
;         else { p0 = __builtin_amdgcn_mfma_f32_32x32x16_bf16(b0, qr[d0], p0, 0, 0, 0); p1 = __builtin_amdgcn_mfma_f32_32x32x16_bf16(b1, qr[d0], p1, 0, 0, 0); } }
; }
.LBB0_829:
	s_waitcnt lgkmcnt(0)
	s_barrier
	ds_read_b128 v[112:115], v72 offset:49152
	ds_read_b128 v[116:119], v73 offset:49152
	ds_read_b128 v[120:123], v74 offset:49152
	ds_read_b128 v[124:127], v75 offset:49152
	ds_read_b128 v[190:193], v72 offset:53248
	ds_read_b128 v[202:205], v73 offset:53248
	ds_read_b128 v[234:237], v74 offset:53248
	ds_read_b128 v[238:241], v75 offset:53248
	global_load_dwordx4 v[178:181], v[66:67], off
	global_load_dwordx4 v[182:185], v[68:69], off
	global_load_dwordx4 v[186:189], v[70:71], off
	v_exp_f32_e32 v208, v152
	v_exp_f32_e32 v209, v153
	v_add_f32_e32 v152, v128, v129
	v_add_f32_e32 v153, v130, v131
	s_waitcnt lgkmcnt(7)
	v_mfma_f32_32x32x16_bf16 v[96:111], v[112:115], v[162:165], v[80:95]
	v_exp_f32_e32 v210, v154
	v_add_f32_e32 v152, v152, v153
	v_add_f32_e32 v153, v132, v133
	v_add_f32_e32 v154, v134, v135
	v_exp_f32_e32 v211, v155
	s_waitcnt lgkmcnt(6)
	v_mfma_f32_32x32x16_bf16 v[96:111], v[116:119], v[166:169], v[96:111]
	v_add_f32_e32 v153, v153, v154
	v_add_f32_e32 v154, v136, v137
	v_add_f32_e32 v155, v138, v139
	v_add_f32_e32 v154, v154, v155
	v_add_f32_e32 v155, v140, v141
	s_waitcnt lgkmcnt(5)
	v_mfma_f32_32x32x16_bf16 v[96:111], v[120:123], v[170:173], v[96:111]
	v_exp_f32_e32 v156, v156
	v_exp_f32_e32 v157, v157
	v_exp_f32_e32 v158, v158
	v_exp_f32_e32 v159, v159
	s_waitcnt lgkmcnt(4)
	v_mfma_f32_32x32x16_bf16 v[96:111], v[124:127], v[174:177], v[96:111]
	s_waitcnt lgkmcnt(3)
	v_mfma_f32_32x32x16_bf16 v[112:127], v[190:193], v[162:165], v[80:95]
	v_add_f32_e32 v190, v142, v143
	v_add_f32_e32 v155, v155, v190
	v_add_f32_e32 v190, v144, v145
	v_add_f32_e32 v191, v146, v147
	v_add_f32_e32 v190, v190, v191
	v_add_f32_e32 v152, v152, v190
	v_add_f32_e32 v190, v148, v149
	s_waitcnt lgkmcnt(2)
	v_mfma_f32_32x32x16_bf16 v[112:127], v[202:205], v[166:169], v[112:127]
	v_lshl_add_u32 v205, s42, 14, v217
	ds_read_b64_tr_b16 v[64:65], v205 offset:0
	ds_read_b64_tr_b16 v[66:67], v205 offset:0x800
	ds_read_b64_tr_b16 v[68:69], v205 offset:0x1000
	ds_read_b64_tr_b16 v[70:71], v205 offset:0x1800
	ds_read_b64_tr_b16 v[72:73], v205 offset:0x2000
	ds_read_b64_tr_b16 v[74:75], v205 offset:0x2800
	ds_read_b64_tr_b16 v[76:77], v205 offset:0x3000
	ds_read_b64_tr_b16 v[78:79], v205 offset:0x3800
	v_add_f32_e32 v191, v150, v151
	v_add_f32_e32 v190, v190, v191
	v_add_f32_e32 v153, v153, v190
	v_add_f32_e32 v190, v208, v209
	v_add_f32_e32 v191, v210, v211
	v_add_f32_e32 v190, v190, v191
	v_add_f32_e32 v154, v154, v190
	s_waitcnt lgkmcnt(9)
	v_mfma_f32_32x32x16_bf16 v[112:127], v[234:237], v[170:173], v[112:127]
	v_add_f32_e32 v190, v156, v157
	v_add_f32_e32 v191, v158, v159
	v_add_f32_e32 v190, v190, v191
	v_add_f32_e32 v155, v155, v190
	v_add_f32_e32 v152, v152, v153
	v_add_f32_e32 v153, v154, v155
	v_add_f32_e32 v203, v152, v153
	s_waitcnt lgkmcnt(8)
	v_mfma_f32_32x32x16_bf16 v[112:127], v[238:241], v[174:177], v[112:127]
	v_mov_b32_e32 v204, v203
	v_cvt_pk_bf16_f32 v152, v128, v129
	v_cvt_pk_bf16_f32 v153, v130, v131
	v_cvt_pk_bf16_f32 v154, v132, v133
	v_cvt_pk_bf16_f32 v155, v134, v135
	v_cvt_pk_bf16_f32 v136, v136, v137
	v_cvt_pk_bf16_f32 v137, v138, v139
	v_cvt_pk_bf16_f32 v138, v140, v141
	v_cvt_pk_bf16_f32 v139, v142, v143
	v_permlane32_swap_b32_e32 v152, v154
	v_permlane32_swap_b32_e32 v153, v155
	v_cvt_pk_bf16_f32 v132, v144, v145
	v_cvt_pk_bf16_f32 v133, v146, v147
	v_cvt_pk_bf16_f32 v134, v148, v149
	v_cvt_pk_bf16_f32 v135, v150, v151
	s_waitcnt lgkmcnt(0)
	v_mfma_f32_32x32x16_bf16 v[0:15], v[152:155], v[64:67], v[0:15]
	v_permlane32_swap_b32_e32 v136, v138
	v_permlane32_swap_b32_e32 v137, v139
	v_cvt_pk_bf16_f32 v128, v208, v209
	v_cvt_pk_bf16_f32 v129, v210, v211
	v_cvt_pk_bf16_f32 v130, v156, v157
	v_cvt_pk_bf16_f32 v131, v158, v159
	v_mfma_f32_32x32x16_bf16 v[0:15], v[136:139], v[68:71], v[0:15]
	v_permlane32_swap_b32_e32 v132, v134
	v_permlane32_swap_b32_e32 v133, v135
	ds_read_b64_tr_b16 v[190:191], v205 offset:0x200
	ds_read_b64_tr_b16 v[192:193], v205 offset:0xa00
	ds_read_b64_tr_b16 v[234:235], v205 offset:0x1200
	ds_read_b64_tr_b16 v[236:237], v205 offset:0x1a00
	ds_read_b64_tr_b16 v[238:239], v205 offset:0x2200
	ds_read_b64_tr_b16 v[240:241], v205 offset:0x2a00
	ds_read_b64_tr_b16 v[242:243], v205 offset:0x3200
	ds_read_b64_tr_b16 v[244:245], v205 offset:0x3a00
	v_mfma_f32_32x32x16_bf16 v[0:15], v[132:135], v[72:75], v[0:15]
	v_permlane32_swap_b32_e32 v128, v130
	v_permlane32_swap_b32_e32 v129, v131
	v_permlane32_swap_b32_e32 v203, v204
	v_max_f32_e32 v140, v96, v97
	v_max3_f32 v140, v140, v112, v114
	v_max3_f32 v141, v98, v99, v113
	v_max3_f32 v140, v140, v115, v100
	v_max3_f32 v141, v141, v102, v103
	v_mfma_f32_32x32x16_bf16 v[0:15], v[128:131], v[76:79], v[0:15]
	v_max3_f32 v202, v140, v101, v116
	v_max3_f32 v208, v141, v118, v119
	ds_read_b64_tr_b16 v[156:157], v205 offset:0x400
	ds_read_b64_tr_b16 v[158:159], v205 offset:0xc00
	ds_read_b64_tr_b16 v[148:149], v205 offset:0x1400
	ds_read_b64_tr_b16 v[150:151], v205 offset:0x1c00
	ds_read_b64_tr_b16 v[144:145], v205 offset:0x2400
	ds_read_b64_tr_b16 v[146:147], v205 offset:0x2c00
	ds_read_b64_tr_b16 v[140:141], v205 offset:0x3400
	ds_read_b64_tr_b16 v[142:143], v205 offset:0x3c00
	s_waitcnt lgkmcnt(8)
	v_mfma_f32_32x32x16_bf16 v[48:63], v[152:155], v[190:193], v[48:63]
	v_max3_f32 v190, v202, v117, v104
	v_max3_f32 v191, v208, v106, v107
	v_max3_f32 v190, v190, v105, v120
	v_max3_f32 v191, v191, v122, v123
	v_max3_f32 v190, v190, v121, v108
	v_max3_f32 v191, v191, v110, v111
	v_max3_f32 v190, v190, v109, v124
	v_add_f32_e32 v255, v231, v232
	v_fmac_f32_e32 v255, v215, v230
	v_add_f32_e32 v215, v203, v204
	v_fmac_f32_e32 v215, v255, v233
	v_mfma_f32_32x32x16_bf16 v[48:63], v[136:139], v[234:237], v[48:63]
	v_max3_f32 v191, v191, v126, v127
	v_max3_f32 v190, v190, v125, v191
	v_mov_b32_e32 v191, v190
	s_nop 1
	v_permlane32_swap_b32_e32 v190, v191
	v_mfma_f32_32x32x16_bf16 v[48:63], v[132:135], v[238:241], v[48:63]
	v_max_f32_e32 v234, v190, v191
	s_mov_b32 s2, 0x4138aa3b
	v_cmp_ge_f32_e32 vcc, s2, v234
	v_mfma_f32_32x32x16_bf16 v[48:63], v[128:131], v[242:245], v[48:63]
	s_cmp_eq_u64 vcc, exec
	v_mov_b32_e32 v202, 1.0
	s_cbranch_scc0 .LBB0_837
; #define SBAR() __builtin_amdgcn_sched_barrier(0)
; #define SLOAD(k0) do { vs0 = *reinterpret_cast<const bf16x8*>(&Vh[(size_t)((k0) + sr) * DM + sc]); vs1 = *reinterpret_cast<const bf16x8*>(&Vh[(size_t)((k0) + 32 + sr) * DM + sc]); \
;     ks = *reinterpret_cast<const bf16x8*>(&Kh[(size_t)((k0) + kr) * DM + kc]); } while (0)
; #define SWRITE(s) do { *(bf16x8*)(V_lds + (s) * SHM_V + vst0) = vs0; *(bf16x8*)(V_lds + (s) * SHM_V + vst1) = vs1; *(bf16x8*)(K_lds + (s) * SHM_K64 + kst) = ks; } while (0)
; #define RESC(a) do { if (__any((a) < 1.f)) { if (hi == 0) al_l[r32] = (a); asm volatile("s_waitcnt lgkmcnt(0)" ::: "memory"); \
;     _Pragma("unroll") for (int d = 0; d < 4; ++d) _Pragma("unroll") for (int r = 0; r < 16; ++r) o[d][r] *= al_l[crow(r, hi)]; } } while (0)
; #define ROT() do { s_prev = s_cur; s_cur = s_next; s_next = (s_next == DA_NBUF - 1) ? 0 : s_next + 1; } while (0)
; __device__ __forceinline__ void diff_pass(const bf16_t* __restrict__ Qb, const bf16_t* __restrict__ Kh, const bf16_t* __restrict__ Vh, int seq, char* lds, f32x16 (&o)[4], const int wave_) {
;     ...
;     for (int j = 1; j + 1 < NT; j += 2) {
;         SLOAD((j + 1) * 64);
;         SBAR(); qkt64c(pB0, pB1, K_lds + s_cur * SHM_K64, qr, negm, r32, hi); FIN(pA0, pA1, alA); SBAR();
;         YSEG(pB0, pB1, alB, s_prev);
;         SWRITE(s_next); RESC(alB); __syncthreads(); ROT();
;         SLOAD((j + 2) * 64);
;         SBAR(); qkt64c(pA0, pA1, K_lds + s_cur * SHM_K64, qr, negm, r32, hi); FIN(pB0, pB1, alB); SBAR();
;         YSEG(pA0, pA1, alA, s_prev);
;         SWRITE(s_next); RESC(alA); __syncthreads(); ROT();
.LBB0_830:
	ds_read_b64_tr_b16 v[190:191], v205 offset:0x600
	ds_read_b64_tr_b16 v[192:193], v205 offset:0xe00
	ds_read_b64_tr_b16 v[234:235], v205 offset:0x1600
	ds_read_b64_tr_b16 v[236:237], v205 offset:0x1e00
	ds_read_b64_tr_b16 v[238:239], v205 offset:0x2600
	ds_read_b64_tr_b16 v[240:241], v205 offset:0x2e00
	ds_read_b64_tr_b16 v[242:243], v205 offset:0x3600
	ds_read_b64_tr_b16 v[244:245], v205 offset:0x3e00
	s_add_i32 s2, s41, 1
	s_waitcnt lgkmcnt(8)
	s_cmp_lg_u32 s41, 2
	s_cselect_b32 s42, s2, 0
	s_lshl_b32 s3, s42, 13
	v_mfma_f32_32x32x16_bf16 v[32:47], v[152:155], v[156:159], v[32:47]
	v_exp_f32_e32 v96, v96
	v_exp_f32_e32 v97, v97
	v_exp_f32_e32 v98, v98
	s_mov_b64 s[8:9], 0x40000
	v_lshl_add_u64 v[198:199], v[198:199], 0, s[8:9]
	v_lshl_add_u64 v[200:201], v[200:201], 0, s[8:9]
	v_mfma_f32_32x32x16_bf16 v[32:47], v[136:139], v[148:151], v[32:47]
	v_exp_f32_e32 v99, v99
	v_exp_f32_e32 v100, v100
	v_exp_f32_e32 v101, v101
	v_mfma_f32_32x32x16_bf16 v[32:47], v[132:135], v[144:147], v[32:47]
	v_exp_f32_e32 v102, v102
	v_exp_f32_e32 v103, v103
	v_exp_f32_e32 v104, v104
	v_mfma_f32_32x32x16_bf16 v[32:47], v[128:131], v[140:143], v[32:47]
	v_exp_f32_e32 v105, v105
	v_exp_f32_e32 v106, v106
	v_exp_f32_e32 v107, v107
	s_waitcnt lgkmcnt(0)
	s_lshl_b32 s2, s42, 14
	s_add_i32 s2, s2, 0
	v_add_u32_e32 v64, s2, v218
	s_waitcnt vmcnt(2)
	ds_write_b128 v64, v[178:181]
	v_add_u32_e32 v64, s2, v219
	s_waitcnt vmcnt(1)
	ds_write_b128 v64, v[182:185]
	v_lshl_add_u32 v64, s42, 13, v221
	s_waitcnt vmcnt(0)
	ds_write_b128 v64, v[186:189] offset:49152
	v_mfma_f32_32x32x16_bf16 v[16:31], v[152:155], v[190:193], v[16:31]
	v_exp_f32_e32 v108, v108
	v_exp_f32_e32 v109, v109
	v_exp_f32_e32 v110, v110
	v_add_u32_e32 v72, s3, v223
	v_add_u32_e32 v73, s3, v226
	v_mfma_f32_32x32x16_bf16 v[16:31], v[136:139], v[234:237], v[16:31]
	v_exp_f32_e32 v111, v111
	v_exp_f32_e32 v112, v112
	v_exp_f32_e32 v113, v113
	v_cmp_gt_f32_e32 vcc, 1.0, v202
	v_add_u32_e32 v74, s3, v228
	v_add_u32_e32 v75, s3, v229
	v_mfma_f32_32x32x16_bf16 v[16:31], v[132:135], v[238:241], v[16:31]
	v_exp_f32_e32 v114, v114
	v_exp_f32_e32 v115, v115
	v_exp_f32_e32 v116, v116
	v_mfma_f32_32x32x16_bf16 v[16:31], v[128:131], v[242:245], v[16:31]
	v_exp_f32_e32 v117, v117
	v_exp_f32_e32 v118, v118
	v_exp_f32_e32 v119, v119
	s_cbranch_vccz .LBB0_834
	s_and_saveexec_b64 s[12:13], s[0:1]
	ds_write_b32 v214, v202 offset:128
	s_or_b64 exec, exec, s[12:13]
	s_waitcnt lgkmcnt(0)
	v_add_u32_e32 v140, v213, v160
	ds_read_b128 v[128:131], v140 offset:224
	ds_read_b128 v[132:135], v140 offset:192
	ds_read_b128 v[136:139], v140 offset:160
	ds_read_b128 v[140:143], v140 offset:128
	s_waitcnt lgkmcnt(3)
	v_pk_mul_f32 v[12:13], v[12:13], v[128:129]
	s_waitcnt lgkmcnt(2)
	v_pk_mul_f32 v[8:9], v[8:9], v[132:133]
	s_waitcnt lgkmcnt(1)
	v_pk_mul_f32 v[4:5], v[4:5], v[136:137]
	v_pk_mul_f32 v[14:15], v[14:15], v[130:131]
	v_pk_mul_f32 v[10:11], v[10:11], v[134:135]
	v_pk_mul_f32 v[6:7], v[6:7], v[138:139]
	s_waitcnt lgkmcnt(0)
	v_pk_mul_f32 v[2:3], v[2:3], v[142:143]
	v_pk_mul_f32 v[0:1], v[0:1], v[140:141]
	v_pk_mul_f32 v[60:61], v[60:61], v[128:129]
	v_pk_mul_f32 v[56:57], v[56:57], v[132:133]
	v_pk_mul_f32 v[52:53], v[52:53], v[136:137]
	v_pk_mul_f32 v[62:63], v[62:63], v[130:131]
	v_pk_mul_f32 v[58:59], v[58:59], v[134:135]
	v_pk_mul_f32 v[54:55], v[54:55], v[138:139]
	v_pk_mul_f32 v[50:51], v[50:51], v[142:143]
	v_pk_mul_f32 v[48:49], v[48:49], v[140:141]
	v_pk_mul_f32 v[44:45], v[44:45], v[128:129]
	v_pk_mul_f32 v[40:41], v[40:41], v[132:133]
	v_pk_mul_f32 v[36:37], v[36:37], v[136:137]
	v_pk_mul_f32 v[46:47], v[46:47], v[130:131]
	v_pk_mul_f32 v[42:43], v[42:43], v[134:135]
	v_pk_mul_f32 v[38:39], v[38:39], v[138:139]
	v_pk_mul_f32 v[34:35], v[34:35], v[142:143]
	v_pk_mul_f32 v[32:33], v[32:33], v[140:141]
	v_pk_mul_f32 v[28:29], v[28:29], v[128:129]
	v_pk_mul_f32 v[24:25], v[24:25], v[132:133]
	v_pk_mul_f32 v[20:21], v[20:21], v[136:137]
	v_pk_mul_f32 v[30:31], v[30:31], v[130:131]
	v_pk_mul_f32 v[26:27], v[26:27], v[134:135]
	v_pk_mul_f32 v[22:23], v[22:23], v[138:139]
	v_pk_mul_f32 v[18:19], v[18:19], v[142:143]
	v_pk_mul_f32 v[16:17], v[16:17], v[140:141]
.LBB0_834:
	s_add_i32 s2, s42, 1
	s_cmp_lg_u32 s42, 2
	s_cselect_b32 s2, s2, 0
	s_add_i32 s40, s40, 2
	s_cmp_gt_u32 s40, 28
	v_mov_b32_e32 v230, v202
	s_mov_b32 s12, s41
	s_mov_b32 s41, s2
	s_waitcnt lgkmcnt(0)
	s_barrier
	s_cbranch_scc1 .LBB0_838
	s_branch .Latt9_p1_top

; __device__ __forceinline__ void qkt64c(f32x16& p0, f32x16& p1, const char* Ks, const bf16x8* qr, const f32x16& cinit, int r32, int hi) {
; #pragma unroll
;     for (int d0 = 0; d0 < 4; ++d0) { const int cb = (d0 * 16 + hi * 8) * 2;
;         const bf16x8 b0 = *reinterpret_cast<const bf16x8*>(Ks + kswz<64>(r32, cb));
;         const bf16x8 b1 = *reinterpret_cast<const bf16x8*>(Ks + kswz<64>(32 + r32, cb));
;         if (d0 == 0) { p0 = __builtin_amdgcn_mfma_f32_32x32x16_bf16(b0, qr[0], cinit, 0, 0, 0); p1 = __builtin_amdgcn_mfma_f32_32x32x16_bf16(b1, qr[0], cinit, 0, 0, 0); }
;         else { p0 = __builtin_amdgcn_mfma_f32_32x32x16_bf16(b0, qr[d0], p0, 0, 0, 0); p1 = __builtin_amdgcn_mfma_f32_32x32x16_bf16(b1, qr[d0], p1, 0, 0, 0); } }
; }
.LBB0_846:
	s_lshl_b32 s2, s30, 13
	s_add_i32 s2, s2, 0
	v_add_u32_e32 v72, s2, v227
	v_add_u32_e32 v73, s2, v231
	v_add_u32_e32 v74, s2, v232
	v_add_u32_e32 v75, s2, v233
.Latt9_p2_top:
	ds_read_b128 v[144:147], v72 offset:49152
	ds_read_b128 v[148:151], v73 offset:49152
	ds_read_b128 v[152:155], v74 offset:49152
	ds_read_b128 v[156:159], v75 offset:49152
	ds_read_b128 v[190:193], v72 offset:53248
	ds_read_b128 v[236:239], v73 offset:53248
	ds_read_b128 v[240:243], v74 offset:53248
	ds_read_b128 v[244:247], v75 offset:53248
	v_lshl_add_u64 v[202:203], v[200:201], 0, s[64:65]
	s_mov_b32 s2, 0x8a40000
	v_add_co_u32_e32 v64, vcc, s2, v202
	s_mov_b32 s2, 0x8a50000
	s_nop 0
	v_addc_co_u32_e32 v65, vcc, 0, v203, vcc
	v_add_co_u32_e32 v66, vcc, s2, v202
	v_lshl_add_u64 v[204:205], v[198:199], 0, s[64:65]
	s_nop 0
	v_addc_co_u32_e32 v67, vcc, 0, v203, vcc
	s_mov_b32 s2, 0x6a40000
	global_load_dwordx4 v[178:181], v[64:65], off
	global_load_dwordx4 v[182:185], v[66:67], off
	v_add_co_u32_e32 v64, vcc, s2, v204
	s_nop 1
	v_addc_co_u32_e32 v65, vcc, 0, v205, vcc
	global_load_dwordx4 v[186:189], v[64:65], off offset:128
	v_exp_f32_e32 v208, v120
	v_exp_f32_e32 v209, v121
	v_add_f32_e32 v120, v96, v97
	v_add_f32_e32 v121, v98, v99
	s_waitcnt lgkmcnt(7)
	v_mfma_f32_32x32x16_bf16 v[128:143], v[144:147], v[162:165], v[80:95]
	v_exp_f32_e32 v210, v122
	v_add_f32_e32 v120, v120, v121
	v_add_f32_e32 v121, v100, v101
	v_add_f32_e32 v122, v102, v103
	v_exp_f32_e32 v211, v123
	s_waitcnt lgkmcnt(6)
	v_mfma_f32_32x32x16_bf16 v[128:143], v[148:151], v[166:169], v[128:143]
	v_add_f32_e32 v121, v121, v122
	v_add_f32_e32 v122, v104, v105
	v_add_f32_e32 v123, v106, v107
	v_add_f32_e32 v122, v122, v123
	v_add_f32_e32 v123, v108, v109
	s_waitcnt lgkmcnt(5)
	v_mfma_f32_32x32x16_bf16 v[128:143], v[152:155], v[170:173], v[128:143]
	v_exp_f32_e32 v124, v124
	v_exp_f32_e32 v125, v125
	v_exp_f32_e32 v126, v126
	v_exp_f32_e32 v127, v127
	v_cvt_pk_bf16_f32 v96, v96, v97
	s_waitcnt lgkmcnt(4)
	v_mfma_f32_32x32x16_bf16 v[128:143], v[156:159], v[174:177], v[128:143]
	v_cvt_pk_bf16_f32 v97, v98, v99
	v_cvt_pk_bf16_f32 v98, v100, v101
	v_cvt_pk_bf16_f32 v99, v102, v103
	s_nop 0
	v_permlane32_swap_b32_e32 v96, v98
	s_waitcnt lgkmcnt(3)
	v_mfma_f32_32x32x16_bf16 v[144:159], v[190:193], v[162:165], v[80:95]
	v_add_f32_e32 v190, v110, v111
	v_add_f32_e32 v123, v123, v190
	v_add_f32_e32 v190, v112, v113
	v_add_f32_e32 v191, v114, v115
	v_add_f32_e32 v190, v190, v191
	v_add_f32_e32 v120, v190, v120
	v_add_f32_e32 v190, v116, v117
	s_waitcnt lgkmcnt(2)
	v_mfma_f32_32x32x16_bf16 v[144:159], v[236:239], v[166:169], v[144:159]
	v_lshl_add_u32 v238, s12, 14, v221
	ds_read_b64_tr_b16 v[64:65], v238 offset:0
	ds_read_b64_tr_b16 v[66:67], v238 offset:0x800
	ds_read_b64_tr_b16 v[68:69], v238 offset:0x1000
	ds_read_b64_tr_b16 v[70:71], v238 offset:0x1800
	ds_read_b64_tr_b16 v[72:73], v238 offset:0x2000
	ds_read_b64_tr_b16 v[74:75], v238 offset:0x2800
	ds_read_b64_tr_b16 v[76:77], v238 offset:0x3000
	ds_read_b64_tr_b16 v[78:79], v238 offset:0x3800
	v_add_f32_e32 v191, v118, v119
	v_add_f32_e32 v190, v190, v191
	v_add_f32_e32 v121, v190, v121
	v_add_f32_e32 v190, v208, v209
	v_add_f32_e32 v191, v210, v211
	v_add_f32_e32 v190, v190, v191
	v_add_f32_e32 v122, v122, v190
	s_waitcnt lgkmcnt(9)
	v_mfma_f32_32x32x16_bf16 v[144:159], v[240:243], v[170:173], v[144:159]
	v_add_f32_e32 v190, v124, v125
	v_add_f32_e32 v191, v126, v127
	v_add_f32_e32 v190, v190, v191
	v_add_f32_e32 v123, v123, v190
	v_add_f32_e32 v120, v120, v121
	v_add_f32_e32 v121, v122, v123
	v_add_f32_e32 v235, v120, v121
	s_waitcnt lgkmcnt(8)
	v_mfma_f32_32x32x16_bf16 v[144:159], v[244:247], v[174:177], v[144:159]
	v_mov_b32_e32 v236, v235
	v_cvt_pk_bf16_f32 v120, v104, v105
	v_cvt_pk_bf16_f32 v121, v106, v107
	v_cvt_pk_bf16_f32 v122, v108, v109
	v_cvt_pk_bf16_f32 v123, v110, v111
	v_permlane32_swap_b32_e32 v97, v99
	v_cvt_pk_bf16_f32 v104, v112, v113
	v_cvt_pk_bf16_f32 v105, v114, v115
	v_cvt_pk_bf16_f32 v106, v116, v117
	v_cvt_pk_bf16_f32 v107, v118, v119
	s_waitcnt lgkmcnt(0)
	v_mfma_f32_32x32x16_bf16 v[0:15], v[96:99], v[64:67], v[0:15]
	v_permlane32_swap_b32_e32 v120, v122
	v_permlane32_swap_b32_e32 v121, v123
	v_cvt_pk_bf16_f32 v100, v208, v209
	v_cvt_pk_bf16_f32 v101, v210, v211
	v_cvt_pk_bf16_f32 v102, v124, v125
	v_cvt_pk_bf16_f32 v103, v126, v127
	v_mfma_f32_32x32x16_bf16 v[0:15], v[120:123], v[68:71], v[0:15]
	v_permlane32_swap_b32_e32 v104, v106
	v_permlane32_swap_b32_e32 v105, v107
	ds_read_b64_tr_b16 v[190:191], v238 offset:0x200
	ds_read_b64_tr_b16 v[192:193], v238 offset:0xa00
	ds_read_b64_tr_b16 v[240:241], v238 offset:0x1200
	ds_read_b64_tr_b16 v[242:243], v238 offset:0x1a00
	ds_read_b64_tr_b16 v[244:245], v238 offset:0x2200
	ds_read_b64_tr_b16 v[246:247], v238 offset:0x2a00
	ds_read_b64_tr_b16 v[208:209], v238 offset:0x3200
	ds_read_b64_tr_b16 v[210:211], v238 offset:0x3a00
	v_mfma_f32_32x32x16_bf16 v[0:15], v[104:107], v[72:75], v[0:15]
	v_permlane32_swap_b32_e32 v100, v102
	v_permlane32_swap_b32_e32 v101, v103
	v_permlane32_swap_b32_e32 v235, v236
	v_max_f32_e32 v108, v128, v129
	v_max3_f32 v108, v108, v144, v146
	v_max3_f32 v109, v130, v131, v145
	v_max3_f32 v108, v108, v147, v132
	v_max3_f32 v109, v109, v134, v135
	v_mfma_f32_32x32x16_bf16 v[0:15], v[100:103], v[76:79], v[0:15]
	v_max3_f32 v237, v108, v133, v148
	v_max3_f32 v239, v109, v150, v151
	ds_read_b64_tr_b16 v[124:125], v238 offset:0x400
	ds_read_b64_tr_b16 v[126:127], v238 offset:0xc00
	ds_read_b64_tr_b16 v[116:117], v238 offset:0x1400
	ds_read_b64_tr_b16 v[118:119], v238 offset:0x1c00
	ds_read_b64_tr_b16 v[112:113], v238 offset:0x2400
	ds_read_b64_tr_b16 v[114:115], v238 offset:0x2c00
	ds_read_b64_tr_b16 v[108:109], v238 offset:0x3400
	ds_read_b64_tr_b16 v[110:111], v238 offset:0x3c00
	s_waitcnt lgkmcnt(8)
	v_mfma_f32_32x32x16_bf16 v[48:63], v[96:99], v[190:193], v[48:63]
	v_max3_f32 v190, v237, v149, v136
	v_max3_f32 v191, v239, v138, v139
	v_max3_f32 v190, v190, v137, v152
	v_max3_f32 v191, v191, v154, v155
	v_max3_f32 v190, v190, v153, v140
	v_max3_f32 v191, v191, v142, v143
	v_max3_f32 v190, v190, v141, v156
	v_mfma_f32_32x32x16_bf16 v[48:63], v[120:123], v[240:243], v[48:63]
	v_max3_f32 v191, v191, v158, v159
	v_max3_f32 v190, v190, v157, v191
	v_mov_b32_e32 v191, v190
	s_nop 1
	v_permlane32_swap_b32_e32 v190, v191
	v_mfma_f32_32x32x16_bf16 v[48:63], v[104:107], v[244:247], v[48:63]
	v_max_f32_e32 v237, v190, v191
	s_mov_b32 s2, 0x4138aa3b
	v_cmp_ge_f32_e32 vcc, s2, v237
	v_mfma_f32_32x32x16_bf16 v[48:63], v[100:103], v[208:211], v[48:63]
	s_cmp_eq_u64 vcc, exec
	s_cbranch_scc0 .LBB0_859
	v_mov_b32_e32 v237, 1.0
.LBB0_848:
	ds_read_b64_tr_b16 v[190:191], v238 offset:0x600
	ds_read_b64_tr_b16 v[192:193], v238 offset:0xe00
	ds_read_b64_tr_b16 v[208:209], v238 offset:0x1600
	ds_read_b64_tr_b16 v[210:211], v238 offset:0x1e00
	ds_read_b64_tr_b16 v[240:241], v238 offset:0x2600
	ds_read_b64_tr_b16 v[242:243], v238 offset:0x2e00
	ds_read_b64_tr_b16 v[244:245], v238 offset:0x3600
	ds_read_b64_tr_b16 v[246:247], v238 offset:0x3e00
	s_waitcnt lgkmcnt(8)
	v_mfma_f32_32x32x16_bf16 v[32:47], v[96:99], v[124:127], v[32:47]
	v_exp_f32_e32 v128, v128
	v_exp_f32_e32 v129, v129
	v_exp_f32_e32 v130, v130
	v_add_co_u32_e32 v66, vcc, 0x8a60000, v202
	s_nop 1
	v_addc_co_u32_e32 v67, vcc, 0, v203, vcc
	v_mfma_f32_32x32x16_bf16 v[32:47], v[120:123], v[116:119], v[32:47]
	v_exp_f32_e32 v131, v131
	v_exp_f32_e32 v132, v132
	v_exp_f32_e32 v133, v133
	v_add_co_u32_e32 v68, vcc, 0x8a70000, v202
	s_nop 1
	v_addc_co_u32_e32 v69, vcc, 0, v203, vcc
	v_mfma_f32_32x32x16_bf16 v[32:47], v[104:107], v[112:115], v[32:47]
	v_exp_f32_e32 v134, v134
	v_exp_f32_e32 v135, v135
	v_exp_f32_e32 v136, v136
	v_add_co_u32_e32 v70, vcc, 0x6a60000, v204
	s_nop 1
	v_addc_co_u32_e32 v71, vcc, 0, v205, vcc
	v_mfma_f32_32x32x16_bf16 v[32:47], v[100:103], v[108:111], v[32:47]
	v_exp_f32_e32 v137, v137
	v_exp_f32_e32 v138, v138
	v_exp_f32_e32 v139, v139
	s_waitcnt lgkmcnt(0)
	s_lshl_b32 s2, s29, 14
	s_add_i32 s2, s2, 0
	v_add_u32_e32 v64, s2, v222
	s_lshl_b32 s3, s29, 13
	s_waitcnt vmcnt(2)
	ds_write_b128 v64, v[178:181]
	v_add_u32_e32 v64, s2, v223
	s_sub_i32 s2, s2, s3
	s_waitcnt vmcnt(1)
	ds_write_b128 v64, v[182:185]
	v_add_u32_e32 v64, s2, v224
	s_waitcnt vmcnt(0)
	ds_write_b128 v64, v[186:189] offset:49152
	v_mfma_f32_32x32x16_bf16 v[16:31], v[96:99], v[190:193], v[16:31]
	v_exp_f32_e32 v140, v140
	v_exp_f32_e32 v141, v141
	v_exp_f32_e32 v142, v142
	v_add_u32_e32 v72, s2, v227
	v_add_u32_e32 v73, s2, v231
	v_mfma_f32_32x32x16_bf16 v[16:31], v[120:123], v[208:211], v[16:31]
	v_exp_f32_e32 v143, v143
	v_exp_f32_e32 v144, v144
	v_exp_f32_e32 v145, v145
	v_cmp_gt_f32_e32 vcc, 1.0, v237
	v_add_u32_e32 v74, s2, v232
	v_add_u32_e32 v75, s2, v233
	v_mfma_f32_32x32x16_bf16 v[16:31], v[104:107], v[240:243], v[16:31]
	v_exp_f32_e32 v146, v146
	v_exp_f32_e32 v147, v147
	v_exp_f32_e32 v148, v148
	v_mfma_f32_32x32x16_bf16 v[16:31], v[100:103], v[244:247], v[16:31]
	v_exp_f32_e32 v149, v149
	v_exp_f32_e32 v150, v150
	v_exp_f32_e32 v151, v151
	s_cbranch_vccz .LBB0_852
	s_and_saveexec_b64 s[10:11], s[0:1]
	ds_write_b32 v218, v237 offset:128
	s_or_b64 exec, exec, s[10:11]
	s_waitcnt lgkmcnt(0)
	v_add_u32_e32 v108, v217, v160
	ds_read_b128 v[96:99], v108 offset:224
	ds_read_b128 v[100:103], v108 offset:192
	ds_read_b128 v[104:107], v108 offset:160
	ds_read_b128 v[108:111], v108 offset:128
	s_waitcnt lgkmcnt(3)
	v_pk_mul_f32 v[12:13], v[12:13], v[96:97]
	s_waitcnt lgkmcnt(2)
	v_pk_mul_f32 v[8:9], v[8:9], v[100:101]
	s_waitcnt lgkmcnt(1)
	v_pk_mul_f32 v[4:5], v[4:5], v[104:105]
	v_pk_mul_f32 v[14:15], v[14:15], v[98:99]
	v_pk_mul_f32 v[10:11], v[10:11], v[102:103]
	v_pk_mul_f32 v[6:7], v[6:7], v[106:107]
	s_waitcnt lgkmcnt(0)
	v_pk_mul_f32 v[2:3], v[2:3], v[110:111]
	v_pk_mul_f32 v[0:1], v[0:1], v[108:109]
	v_pk_mul_f32 v[60:61], v[60:61], v[96:97]
	v_pk_mul_f32 v[56:57], v[56:57], v[100:101]
	v_pk_mul_f32 v[52:53], v[52:53], v[104:105]
	v_pk_mul_f32 v[62:63], v[62:63], v[98:99]
	v_pk_mul_f32 v[58:59], v[58:59], v[102:103]
	v_pk_mul_f32 v[54:55], v[54:55], v[106:107]
	v_pk_mul_f32 v[50:51], v[50:51], v[110:111]
	v_pk_mul_f32 v[48:49], v[48:49], v[108:109]
	v_pk_mul_f32 v[44:45], v[44:45], v[96:97]
	v_pk_mul_f32 v[40:41], v[40:41], v[100:101]
	v_pk_mul_f32 v[36:37], v[36:37], v[104:105]
	v_pk_mul_f32 v[46:47], v[46:47], v[98:99]
	v_pk_mul_f32 v[42:43], v[42:43], v[102:103]
	v_pk_mul_f32 v[38:39], v[38:39], v[106:107]
	v_pk_mul_f32 v[34:35], v[34:35], v[110:111]
	v_pk_mul_f32 v[32:33], v[32:33], v[108:109]
	v_pk_mul_f32 v[28:29], v[28:29], v[96:97]
	v_pk_mul_f32 v[24:25], v[24:25], v[100:101]
	v_pk_mul_f32 v[20:21], v[20:21], v[104:105]
	v_pk_mul_f32 v[30:31], v[30:31], v[98:99]
	v_pk_mul_f32 v[26:27], v[26:27], v[102:103]
	v_pk_mul_f32 v[22:23], v[22:23], v[106:107]
	v_pk_mul_f32 v[18:19], v[18:19], v[110:111]
	v_pk_mul_f32 v[16:17], v[16:17], v[108:109]
; __device__ __forceinline__ void qkt64c(f32x16& p0, f32x16& p1, const char* Ks, const bf16x8* qr, const f32x16& cinit, int r32, int hi) {
; #pragma unroll
;     for (int d0 = 0; d0 < 4; ++d0) { const int cb = (d0 * 16 + hi * 8) * 2;
;         const bf16x8 b0 = *reinterpret_cast<const bf16x8*>(Ks + kswz<64>(r32, cb));
;         const bf16x8 b1 = *reinterpret_cast<const bf16x8*>(Ks + kswz<64>(32 + r32, cb));
;         if (d0 == 0) { p0 = __builtin_amdgcn_mfma_f32_32x32x16_bf16(b0, qr[0], cinit, 0, 0, 0); p1 = __builtin_amdgcn_mfma_f32_32x32x16_bf16(b1, qr[0], cinit, 0, 0, 0); }
;         else { p0 = __builtin_amdgcn_mfma_f32_32x32x16_bf16(b0, qr[d0], p0, 0, 0, 0); p1 = __builtin_amdgcn_mfma_f32_32x32x16_bf16(b1, qr[d0], p1, 0, 0, 0); } }
; }
.LBB0_852:
	s_waitcnt lgkmcnt(0)
	s_barrier
	ds_read_b128 v[112:115], v72 offset:49152
	ds_read_b128 v[116:119], v73 offset:49152
	ds_read_b128 v[120:123], v74 offset:49152
	ds_read_b128 v[124:127], v75 offset:49152
	ds_read_b128 v[190:193], v72 offset:53248
	ds_read_b128 v[202:205], v73 offset:53248
	ds_read_b128 v[208:211], v74 offset:53248
	ds_read_b128 v[238:241], v75 offset:53248
	global_load_dwordx4 v[178:181], v[66:67], off
	global_load_dwordx4 v[182:185], v[68:69], off
	global_load_dwordx4 v[186:189], v[70:71], off offset:128
	v_exp_f32_e32 v242, v152
	v_exp_f32_e32 v243, v153
	v_add_f32_e32 v152, v128, v129
	v_add_f32_e32 v153, v130, v131
	s_waitcnt lgkmcnt(7)
	v_mfma_f32_32x32x16_bf16 v[96:111], v[112:115], v[162:165], v[80:95]
	v_exp_f32_e32 v244, v154
	v_add_f32_e32 v152, v152, v153
	v_add_f32_e32 v153, v132, v133
	v_add_f32_e32 v154, v134, v135
	v_exp_f32_e32 v245, v155
	s_waitcnt lgkmcnt(6)
	v_mfma_f32_32x32x16_bf16 v[96:111], v[116:119], v[166:169], v[96:111]
	v_add_f32_e32 v153, v153, v154
	v_add_f32_e32 v154, v136, v137
	v_add_f32_e32 v155, v138, v139
	v_add_f32_e32 v154, v154, v155
	v_add_f32_e32 v155, v140, v141
	s_waitcnt lgkmcnt(5)
	v_mfma_f32_32x32x16_bf16 v[96:111], v[120:123], v[170:173], v[96:111]
	v_exp_f32_e32 v156, v156
	v_exp_f32_e32 v157, v157
	v_exp_f32_e32 v158, v158
	v_exp_f32_e32 v159, v159
	s_waitcnt lgkmcnt(4)
	v_mfma_f32_32x32x16_bf16 v[96:111], v[124:127], v[174:177], v[96:111]
	s_waitcnt lgkmcnt(3)
	v_mfma_f32_32x32x16_bf16 v[112:127], v[190:193], v[162:165], v[80:95]
	v_add_f32_e32 v190, v142, v143
	v_add_f32_e32 v155, v155, v190
	v_add_f32_e32 v190, v144, v145
	v_add_f32_e32 v191, v146, v147
	v_add_f32_e32 v190, v190, v191
	v_add_f32_e32 v152, v152, v190
	v_add_f32_e32 v190, v148, v149
	s_waitcnt lgkmcnt(2)
	v_mfma_f32_32x32x16_bf16 v[112:127], v[202:205], v[166:169], v[112:127]
	v_lshl_add_u32 v205, s30, 14, v221
	ds_read_b64_tr_b16 v[64:65], v205 offset:0
	ds_read_b64_tr_b16 v[66:67], v205 offset:0x800
	ds_read_b64_tr_b16 v[68:69], v205 offset:0x1000
	ds_read_b64_tr_b16 v[70:71], v205 offset:0x1800
	ds_read_b64_tr_b16 v[72:73], v205 offset:0x2000
	ds_read_b64_tr_b16 v[74:75], v205 offset:0x2800
	ds_read_b64_tr_b16 v[76:77], v205 offset:0x3000
	ds_read_b64_tr_b16 v[78:79], v205 offset:0x3800
	v_add_f32_e32 v191, v150, v151
	v_add_f32_e32 v190, v190, v191
	v_add_f32_e32 v153, v153, v190
	v_add_f32_e32 v190, v242, v243
	v_add_f32_e32 v191, v244, v245
	v_add_f32_e32 v190, v190, v191
	v_add_f32_e32 v154, v154, v190
	s_waitcnt lgkmcnt(9)
	v_mfma_f32_32x32x16_bf16 v[112:127], v[208:211], v[170:173], v[112:127]
	v_add_f32_e32 v190, v156, v157
	v_add_f32_e32 v191, v158, v159
	v_add_f32_e32 v190, v190, v191
	v_add_f32_e32 v155, v155, v190
	v_add_f32_e32 v152, v152, v153
	v_add_f32_e32 v153, v154, v155
	v_add_f32_e32 v203, v152, v153
	s_waitcnt lgkmcnt(8)
	v_mfma_f32_32x32x16_bf16 v[112:127], v[238:241], v[174:177], v[112:127]
	v_mov_b32_e32 v204, v203
	v_cvt_pk_bf16_f32 v152, v128, v129
	v_cvt_pk_bf16_f32 v153, v130, v131
	v_cvt_pk_bf16_f32 v154, v132, v133
	v_cvt_pk_bf16_f32 v155, v134, v135
	v_cvt_pk_bf16_f32 v136, v136, v137
	v_cvt_pk_bf16_f32 v137, v138, v139
	v_cvt_pk_bf16_f32 v138, v140, v141
	v_cvt_pk_bf16_f32 v139, v142, v143
	v_permlane32_swap_b32_e32 v152, v154
	v_permlane32_swap_b32_e32 v153, v155
	v_cvt_pk_bf16_f32 v132, v144, v145
	v_cvt_pk_bf16_f32 v133, v146, v147
	v_cvt_pk_bf16_f32 v134, v148, v149
	v_cvt_pk_bf16_f32 v135, v150, v151
	s_waitcnt lgkmcnt(0)
	v_mfma_f32_32x32x16_bf16 v[0:15], v[152:155], v[64:67], v[0:15]
	v_permlane32_swap_b32_e32 v136, v138
	v_permlane32_swap_b32_e32 v137, v139
	v_cvt_pk_bf16_f32 v128, v242, v243
	v_cvt_pk_bf16_f32 v129, v244, v245
	v_cvt_pk_bf16_f32 v130, v156, v157
	v_cvt_pk_bf16_f32 v131, v158, v159
	v_mfma_f32_32x32x16_bf16 v[0:15], v[136:139], v[68:71], v[0:15]
	v_permlane32_swap_b32_e32 v132, v134
	v_permlane32_swap_b32_e32 v133, v135
	ds_read_b64_tr_b16 v[190:191], v205 offset:0x200
	ds_read_b64_tr_b16 v[192:193], v205 offset:0xa00
	ds_read_b64_tr_b16 v[208:209], v205 offset:0x1200
	ds_read_b64_tr_b16 v[210:211], v205 offset:0x1a00
	ds_read_b64_tr_b16 v[238:239], v205 offset:0x2200
	ds_read_b64_tr_b16 v[240:241], v205 offset:0x2a00
	ds_read_b64_tr_b16 v[242:243], v205 offset:0x3200
	ds_read_b64_tr_b16 v[244:245], v205 offset:0x3a00
	v_mfma_f32_32x32x16_bf16 v[0:15], v[132:135], v[72:75], v[0:15]
	v_permlane32_swap_b32_e32 v128, v130
	v_permlane32_swap_b32_e32 v129, v131
	v_permlane32_swap_b32_e32 v203, v204
	v_max_f32_e32 v140, v96, v97
	v_max3_f32 v140, v140, v112, v114
	v_max3_f32 v141, v98, v99, v113
	v_max3_f32 v140, v140, v115, v100
	v_max3_f32 v141, v141, v102, v103
	v_mfma_f32_32x32x16_bf16 v[0:15], v[128:131], v[76:79], v[0:15]
	v_max3_f32 v202, v140, v101, v116
	v_max3_f32 v246, v141, v118, v119
	ds_read_b64_tr_b16 v[156:157], v205 offset:0x400
	ds_read_b64_tr_b16 v[158:159], v205 offset:0xc00
	ds_read_b64_tr_b16 v[148:149], v205 offset:0x1400
	ds_read_b64_tr_b16 v[150:151], v205 offset:0x1c00
	ds_read_b64_tr_b16 v[144:145], v205 offset:0x2400
	ds_read_b64_tr_b16 v[146:147], v205 offset:0x2c00
	ds_read_b64_tr_b16 v[140:141], v205 offset:0x3400
	ds_read_b64_tr_b16 v[142:143], v205 offset:0x3c00
	s_waitcnt lgkmcnt(8)
	v_mfma_f32_32x32x16_bf16 v[48:63], v[152:155], v[190:193], v[48:63]
	v_max3_f32 v190, v202, v117, v104
	v_max3_f32 v191, v246, v106, v107
	v_max3_f32 v190, v190, v105, v120
	v_max3_f32 v191, v191, v122, v123
	v_max3_f32 v190, v190, v121, v108
	v_max3_f32 v191, v191, v110, v111
	v_max3_f32 v190, v190, v109, v124
	v_add_f32_e32 v255, v235, v236
	v_fmac_f32_e32 v255, v219, v234
	v_add_f32_e32 v219, v203, v204
	v_fmac_f32_e32 v219, v255, v237
	v_mfma_f32_32x32x16_bf16 v[48:63], v[136:139], v[208:211], v[48:63]
	v_max3_f32 v191, v191, v126, v127
	v_max3_f32 v190, v190, v125, v191
	v_mov_b32_e32 v191, v190
	s_nop 1
	v_permlane32_swap_b32_e32 v190, v191
	v_mfma_f32_32x32x16_bf16 v[48:63], v[132:135], v[238:241], v[48:63]
	v_max_f32_e32 v238, v190, v191
	s_mov_b32 s2, 0x4138aa3b
	v_cmp_ge_f32_e32 vcc, s2, v238
	v_mfma_f32_32x32x16_bf16 v[48:63], v[128:131], v[242:245], v[48:63]
	s_cmp_eq_u64 vcc, exec
	v_mov_b32_e32 v202, 1.0
	s_cbranch_scc0 .LBB0_860
; #define SBAR() __builtin_amdgcn_sched_barrier(0)
; #define SLOAD(k0) do { vs0 = *reinterpret_cast<const bf16x8*>(&Vh[(size_t)((k0) + sr) * DM + sc]); vs1 = *reinterpret_cast<const bf16x8*>(&Vh[(size_t)((k0) + 32 + sr) * DM + sc]); \
;     ks = *reinterpret_cast<const bf16x8*>(&Kh[(size_t)((k0) + kr) * DM + kc]); } while (0)
; #define SWRITE(s) do { *(bf16x8*)(V_lds + (s) * SHM_V + vst0) = vs0; *(bf16x8*)(V_lds + (s) * SHM_V + vst1) = vs1; *(bf16x8*)(K_lds + (s) * SHM_K64 + kst) = ks; } while (0)
; #define RESC(a) do { if (__any((a) < 1.f)) { if (hi == 0) al_l[r32] = (a); asm volatile("s_waitcnt lgkmcnt(0)" ::: "memory"); \
;     _Pragma("unroll") for (int d = 0; d < 4; ++d) _Pragma("unroll") for (int r = 0; r < 16; ++r) o[d][r] *= al_l[crow(r, hi)]; } } while (0)
; #define ROT() do { s_prev = s_cur; s_cur = s_next; s_next = (s_next == DA_NBUF - 1) ? 0 : s_next + 1; } while (0)
; __device__ __forceinline__ void diff_pass(const bf16_t* __restrict__ Qb, const bf16_t* __restrict__ Kh, const bf16_t* __restrict__ Vh, int seq, char* lds, f32x16 (&o)[4], const int wave_) {
;     ...
;     for (int j = 1; j + 1 < NT; j += 2) {
;         SLOAD((j + 1) * 64);
;         SBAR(); qkt64c(pB0, pB1, K_lds + s_cur * SHM_K64, qr, negm, r32, hi); FIN(pA0, pA1, alA); SBAR();
;         YSEG(pB0, pB1, alB, s_prev);
;         SWRITE(s_next); RESC(alB); __syncthreads(); ROT();
;         SLOAD((j + 2) * 64);
;         SBAR(); qkt64c(pA0, pA1, K_lds + s_cur * SHM_K64, qr, negm, r32, hi); FIN(pB0, pB1, alB); SBAR();
;         YSEG(pA0, pA1, alA, s_prev);
;         SWRITE(s_next); RESC(alA); __syncthreads(); ROT();
.LBB0_853:
	ds_read_b64_tr_b16 v[190:191], v205 offset:0x600
	ds_read_b64_tr_b16 v[192:193], v205 offset:0xe00
	ds_read_b64_tr_b16 v[208:209], v205 offset:0x1600
	ds_read_b64_tr_b16 v[210:211], v205 offset:0x1e00
	ds_read_b64_tr_b16 v[238:239], v205 offset:0x2600
	ds_read_b64_tr_b16 v[240:241], v205 offset:0x2e00
	ds_read_b64_tr_b16 v[242:243], v205 offset:0x3600
	ds_read_b64_tr_b16 v[244:245], v205 offset:0x3e00
	s_add_i32 s2, s29, 1
	s_waitcnt lgkmcnt(8)
	s_cmp_lg_u32 s29, 2
	s_cselect_b32 s30, s2, 0
	s_lshl_b32 s3, s30, 13
	v_mfma_f32_32x32x16_bf16 v[32:47], v[152:155], v[156:159], v[32:47]
	v_exp_f32_e32 v96, v96
	v_exp_f32_e32 v97, v97
	v_exp_f32_e32 v98, v98
	s_mov_b64 s[8:9], 0x40000
	v_lshl_add_u64 v[198:199], v[198:199], 0, s[8:9]
	v_lshl_add_u64 v[200:201], v[200:201], 0, s[8:9]
	v_mfma_f32_32x32x16_bf16 v[32:47], v[136:139], v[148:151], v[32:47]
	v_exp_f32_e32 v99, v99
	v_exp_f32_e32 v100, v100
	v_exp_f32_e32 v101, v101
	v_mfma_f32_32x32x16_bf16 v[32:47], v[132:135], v[144:147], v[32:47]
	v_exp_f32_e32 v102, v102
	v_exp_f32_e32 v103, v103
	v_exp_f32_e32 v104, v104
	v_mfma_f32_32x32x16_bf16 v[32:47], v[128:131], v[140:143], v[32:47]
	v_exp_f32_e32 v105, v105
	v_exp_f32_e32 v106, v106
	v_exp_f32_e32 v107, v107
	s_waitcnt lgkmcnt(0)
	s_lshl_b32 s2, s30, 14
	s_add_i32 s2, s2, 0
	v_add_u32_e32 v64, s2, v222
	s_waitcnt vmcnt(2)
	ds_write_b128 v64, v[178:181]
	v_add_u32_e32 v64, s2, v223
	s_waitcnt vmcnt(1)
	ds_write_b128 v64, v[182:185]
	v_lshl_add_u32 v64, s30, 13, v225
	s_waitcnt vmcnt(0)
	ds_write_b128 v64, v[186:189] offset:49152
	v_mfma_f32_32x32x16_bf16 v[16:31], v[152:155], v[190:193], v[16:31]
	v_exp_f32_e32 v108, v108
	v_exp_f32_e32 v109, v109
	v_exp_f32_e32 v110, v110
	v_add_u32_e32 v72, s3, v227
	v_add_u32_e32 v73, s3, v231
	v_mfma_f32_32x32x16_bf16 v[16:31], v[136:139], v[208:211], v[16:31]
	v_exp_f32_e32 v111, v111
	v_exp_f32_e32 v112, v112
	v_exp_f32_e32 v113, v113
	v_cmp_gt_f32_e32 vcc, 1.0, v202
	v_add_u32_e32 v74, s3, v232
	v_add_u32_e32 v75, s3, v233
	v_mfma_f32_32x32x16_bf16 v[16:31], v[132:135], v[238:241], v[16:31]
	v_exp_f32_e32 v114, v114
	v_exp_f32_e32 v115, v115
	v_exp_f32_e32 v116, v116
	v_mfma_f32_32x32x16_bf16 v[16:31], v[128:131], v[242:245], v[16:31]
	v_exp_f32_e32 v117, v117
	v_exp_f32_e32 v118, v118
	v_exp_f32_e32 v119, v119
	s_cbranch_vccz .LBB0_857
	s_and_saveexec_b64 s[10:11], s[0:1]
	ds_write_b32 v218, v202 offset:128
	s_or_b64 exec, exec, s[10:11]
	s_waitcnt lgkmcnt(0)
	v_add_u32_e32 v140, v217, v160
	ds_read_b128 v[128:131], v140 offset:224
	ds_read_b128 v[132:135], v140 offset:192
	ds_read_b128 v[136:139], v140 offset:160
	ds_read_b128 v[140:143], v140 offset:128
	s_waitcnt lgkmcnt(3)
	v_pk_mul_f32 v[12:13], v[12:13], v[128:129]
	s_waitcnt lgkmcnt(2)
	v_pk_mul_f32 v[8:9], v[8:9], v[132:133]
	s_waitcnt lgkmcnt(1)
	v_pk_mul_f32 v[4:5], v[4:5], v[136:137]
	v_pk_mul_f32 v[14:15], v[14:15], v[130:131]
	v_pk_mul_f32 v[10:11], v[10:11], v[134:135]
	v_pk_mul_f32 v[6:7], v[6:7], v[138:139]
	s_waitcnt lgkmcnt(0)
	v_pk_mul_f32 v[2:3], v[2:3], v[142:143]
	v_pk_mul_f32 v[0:1], v[0:1], v[140:141]
	v_pk_mul_f32 v[60:61], v[60:61], v[128:129]
	v_pk_mul_f32 v[56:57], v[56:57], v[132:133]
	v_pk_mul_f32 v[52:53], v[52:53], v[136:137]
	v_pk_mul_f32 v[62:63], v[62:63], v[130:131]
	v_pk_mul_f32 v[58:59], v[58:59], v[134:135]
	v_pk_mul_f32 v[54:55], v[54:55], v[138:139]
	v_pk_mul_f32 v[50:51], v[50:51], v[142:143]
	v_pk_mul_f32 v[48:49], v[48:49], v[140:141]
	v_pk_mul_f32 v[44:45], v[44:45], v[128:129]
	v_pk_mul_f32 v[40:41], v[40:41], v[132:133]
	v_pk_mul_f32 v[36:37], v[36:37], v[136:137]
	v_pk_mul_f32 v[46:47], v[46:47], v[130:131]
	v_pk_mul_f32 v[42:43], v[42:43], v[134:135]
	v_pk_mul_f32 v[38:39], v[38:39], v[138:139]
	v_pk_mul_f32 v[34:35], v[34:35], v[142:143]
	v_pk_mul_f32 v[32:33], v[32:33], v[140:141]
	v_pk_mul_f32 v[28:29], v[28:29], v[128:129]
	v_pk_mul_f32 v[24:25], v[24:25], v[132:133]
	v_pk_mul_f32 v[20:21], v[20:21], v[136:137]
	v_pk_mul_f32 v[30:31], v[30:31], v[130:131]
	v_pk_mul_f32 v[26:27], v[26:27], v[134:135]
	v_pk_mul_f32 v[22:23], v[22:23], v[138:139]
	v_pk_mul_f32 v[18:19], v[18:19], v[142:143]
	v_pk_mul_f32 v[16:17], v[16:17], v[140:141]
.LBB0_857:
	s_add_i32 s2, s30, 1
	s_cmp_lg_u32 s30, 2
	s_cselect_b32 s2, s2, 0
	s_add_i32 s28, s28, 2
	s_cmp_gt_u32 s28, 28
	v_mov_b32_e32 v234, v202
	s_mov_b32 s12, s29
	s_mov_b32 s29, s2
	s_waitcnt lgkmcnt(0)
	s_barrier
	s_cbranch_scc1 .LBB0_861
	s_branch .Latt9_p2_top
